# qkv epilogue: q_s/k_s row-copy ladder de-serialised (four LDS row indices read at once, straight-line exec masking, SGPR-base stores)
# baseline (speedup 1.0000x reference)
.LBB1_52:
	s_or_b64 exec, exec, s[2:3]
	v_lshlrev_b32_e32 v43, 2, v64
	s_waitcnt lgkmcnt(0)
	s_barrier
	ds_read_b32 v36, v43 offset:34816
	ds_read_b32 v37, v43 offset:34944
	ds_read_b32 v38, v43 offset:35072
	ds_read_b32 v39, v43 offset:35200
	v_lshlrev_b32_e32 v1, 3, v0
	v_and_b32_e32 v1, 56, v1
	v_lshlrev_b32_e32 v40, 1, v1
	v_mul_u32_u24_e32 v1, 0x110, v64
	v_add_u32_e32 v41, v1, v40
	s_mov_b64 s[0:1], exec
	s_waitcnt lgkmcnt(0)
	v_cmp_lt_i32_e32 vcc, -1, v36
	s_and_b64 exec, s[0:1], vcc
	ds_read_b128 v[58:61], v41
	ds_read_b128 v[62:65], v41 offset:128
	v_lshl_add_u32 v36, v36, 7, v40
	s_waitcnt lgkmcnt(1)
	global_store_dwordx4 v36, v[58:61], s[12:13]
	s_waitcnt lgkmcnt(0)
	global_store_dwordx4 v36, v[62:65], s[14:15]
	s_mov_b64 exec, s[0:1]
	v_cmp_lt_i32_e32 vcc, -1, v37
	s_and_b64 exec, s[0:1], vcc
	ds_read_b128 v[58:61], v41 offset:8704
	ds_read_b128 v[62:65], v41 offset:8832
	v_lshl_add_u32 v37, v37, 7, v40
	s_waitcnt lgkmcnt(1)
	global_store_dwordx4 v37, v[58:61], s[12:13]
	s_waitcnt lgkmcnt(0)
	global_store_dwordx4 v37, v[62:65], s[14:15]
	s_mov_b64 exec, s[0:1]
	v_cmp_lt_i32_e32 vcc, -1, v38
	s_and_b64 exec, s[0:1], vcc
	ds_read_b128 v[58:61], v41 offset:17408
	ds_read_b128 v[62:65], v41 offset:17536
	v_lshl_add_u32 v38, v38, 7, v40
	s_waitcnt lgkmcnt(1)
	global_store_dwordx4 v38, v[58:61], s[12:13]
	s_waitcnt lgkmcnt(0)
	global_store_dwordx4 v38, v[62:65], s[14:15]
	s_mov_b64 exec, s[0:1]
	v_cmp_lt_i32_e32 vcc, -1, v39
	s_and_b64 exec, s[0:1], vcc
	ds_read_b128 v[58:61], v41 offset:26112
	ds_read_b128 v[62:65], v41 offset:26240
	v_lshl_add_u32 v39, v39, 7, v40
	s_waitcnt lgkmcnt(1)
	global_store_dwordx4 v39, v[58:61], s[12:13]
	s_waitcnt lgkmcnt(0)
	global_store_dwordx4 v39, v[62:65], s[14:15]
	s_mov_b64 exec, s[0:1]
	v_lshl_add_u32 v0, v92, 2, v101
	s_barrier
	ds_write2_b32 v0, v18, v26 offset1:16
	ds_write2_b32 v0, v19, v27 offset0:68 offset1:84
	ds_write2_b32 v0, v20, v28 offset0:136 offset1:152
	ds_write2_b32 v0, v21, v29 offset0:204 offset1:220
	ds_write2_b32 v0, v22, v30 offset0:32 offset1:48
	ds_write2_b32 v0, v23, v31 offset0:100 offset1:116
	ds_write2_b32 v0, v24, v32 offset0:168 offset1:184
	ds_write2_b32 v0, v25, v33 offset0:236 offset1:252
	v_add_u32_e32 v1, 0x1000, v0
	v_add_u32_e32 v0, 0x1400, v0
	ds_write2_b32 v1, v2, v10 offset0:64 offset1:80
	ds_write2_b32 v1, v3, v11 offset0:132 offset1:148
	ds_write2_b32 v1, v4, v12 offset0:200 offset1:216
	ds_write2_b32 v0, v5, v13 offset0:12 offset1:28
	ds_write2_b32 v1, v6, v14 offset0:96 offset1:112
	ds_write2_b32 v1, v7, v15 offset0:164 offset1:180
	ds_write2_b32 v1, v8, v16 offset0:232 offset1:248
	ds_write2_b32 v0, v9, v17 offset0:44 offset1:60
	s_waitcnt lgkmcnt(0)
	s_barrier
	s_and_saveexec_b64 s[0:1], s[4:5]
	s_cbranch_execz .LBB1_62
	v_max3_f32 v0, v55, v54, v53
	v_max3_f32 v0, v0, v52, v51
	v_max3_f32 v0, v0, v50, v49
	v_max3_f32 v0, v0, v35, v48
	v_sub_f32_e32 v1, v55, v0
	v_mul_f32_e32 v1, 0x3fb8aa3b, v1
	v_sub_f32_e32 v2, v54, v0
	v_exp_f32_e32 v1, v1
	v_sub_f32_e32 v3, v53, v0
	v_mul_f32_e32 v2, 0x3fb8aa3b, v2
	v_exp_f32_e32 v2, v2
	v_mul_f32_e32 v3, 0x3fb8aa3b, v3
	v_sub_f32_e32 v5, v52, v0
	v_exp_f32_e32 v3, v3
	v_mul_f32_e32 v5, 0x3fb8aa3b, v5
	v_sub_f32_e32 v6, v51, v0
	v_exp_f32_e32 v5, v5
	v_mul_f32_e32 v6, 0x3fb8aa3b, v6
	v_sub_f32_e32 v7, v50, v0
	v_add_f32_e32 v4, 0, v1
	v_exp_f32_e32 v9, v6
	v_mul_f32_e32 v6, 0x3fb8aa3b, v7
	v_sub_f32_e32 v7, v49, v0
	v_add_f32_e32 v4, v4, v2
	v_exp_f32_e32 v11, v6
	v_mul_f32_e32 v6, 0x3fb8aa3b, v7
	v_sub_f32_e32 v7, v35, v0
	v_add_f32_e32 v4, v4, v3
	v_exp_f32_e32 v13, v6
	v_mul_f32_e32 v6, 0x3fb8aa3b, v7
	v_sub_f32_e32 v0, v48, v0
	v_add_f32_e32 v4, v4, v5
	v_exp_f32_e32 v7, v6
	v_mul_f32_e32 v0, 0x3fb8aa3b, v0
	v_add_f32_e32 v4, v4, v9
	v_exp_f32_e32 v0, v0
	v_add_f32_e32 v4, v4, v11
	v_add_f32_e32 v4, v4, v13
	v_add_f32_e32 v4, v4, v7
	v_add_f32_e32 v4, v4, v0
	v_rcp_f32_e32 v15, v4
	v_ashrrev_i32_e32 v35, 31, v34
	s_movk_i32 s0, 0xc5
	v_mul_f32_e32 v4, v15, v1
	v_mul_f32_e32 v20, v15, v0
	v_mad_u64_u32 v[0:1], s[0:1], v56, s0, v[34:35]
	s_movk_i32 s0, 0x110
	v_mul_f32_e32 v6, v15, v2
	v_mul_lo_u32 v2, v46, s0
	v_lshlrev_b64 v[0:1], 7, v[0:1]
	v_mul_f32_e32 v8, v15, v3
	v_mul_f32_e32 v10, v15, v5
	v_lshl_add_u32 v5, v47, 7, v2
	v_lshl_add_u64 v[0:1], s[6:7], 0, v[0:1]
	v_lshlrev_b32_e32 v2, 6, v47
	v_mov_b32_e32 v3, 0
	v_lshl_add_u64 v[22:23], v[0:1], 0, v[2:3]
	ds_read_b128 v[24:27], v5
	ds_read_b128 v[28:31], v5 offset:16
	ds_read_b128 v[32:35], v5 offset:3808
	ds_read_b128 v[36:39], v5 offset:32
	ds_read_b128 v[0:3], v5 offset:48
	ds_read_b128 v[40:43], v5 offset:7616
	ds_read_b128 v[44:47], v5 offset:3824
	ds_read_b128 v[48:51], v5 offset:11424
	ds_read_b128 v[52:55], v5 offset:7632
	s_waitcnt lgkmcnt(8)
	v_pk_fma_f32 v[24:25], v[4:5], v[24:25], 0 op_sel_hi:[0,1,0]
	s_waitcnt lgkmcnt(6)
	v_pk_fma_f32 v[24:25], v[6:7], v[32:33], v[24:25] op_sel_hi:[0,1,1]
	ds_read_b128 v[56:59], v5 offset:15232
	ds_read_b128 v[60:63], v5 offset:19040
	ds_read_b128 v[64:67], v5 offset:11440
	s_waitcnt lgkmcnt(6)
	v_pk_fma_f32 v[24:25], v[8:9], v[40:41], v[24:25] op_sel_hi:[0,1,1]
	v_mul_f32_e32 v12, v15, v9
	s_waitcnt lgkmcnt(4)
	v_pk_fma_f32 v[24:25], v[10:11], v[48:49], v[24:25] op_sel_hi:[0,1,1]
	v_mul_f32_e32 v14, v15, v11
	s_waitcnt lgkmcnt(2)
	v_pk_fma_f32 v[24:25], v[12:13], v[56:57], v[24:25] op_sel_hi:[0,1,1]
	s_waitcnt lgkmcnt(1)
	v_pk_fma_f32 v[76:77], v[14:15], v[60:61], v[24:25] op_sel_hi:[0,1,1]
	v_pk_fma_f32 v[24:25], v[4:5], v[26:27], 0 op_sel_hi:[0,1,0]
	v_pk_fma_f32 v[24:25], v[6:7], v[34:35], v[24:25] op_sel_hi:[0,1,1]
	v_pk_fma_f32 v[24:25], v[8:9], v[42:43], v[24:25] op_sel_hi:[0,1,1]
	v_pk_fma_f32 v[24:25], v[10:11], v[50:51], v[24:25] op_sel_hi:[0,1,1]
	ds_read_b128 v[68:71], v5 offset:15248
	ds_read_b128 v[72:75], v5 offset:19056
	v_pk_fma_f32 v[24:25], v[12:13], v[58:59], v[24:25] op_sel_hi:[0,1,1]
	v_pk_fma_f32 v[78:79], v[14:15], v[62:63], v[24:25] op_sel_hi:[0,1,1]
	v_pk_fma_f32 v[24:25], v[4:5], v[28:29], 0 op_sel_hi:[0,1,0]
	v_pk_fma_f32 v[24:25], v[6:7], v[44:45], v[24:25] op_sel_hi:[0,1,1]
	v_pk_fma_f32 v[24:25], v[8:9], v[52:53], v[24:25] op_sel_hi:[0,1,1]
	s_waitcnt lgkmcnt(2)
	v_pk_fma_f32 v[24:25], v[10:11], v[64:65], v[24:25] op_sel_hi:[0,1,1]
	s_waitcnt lgkmcnt(1)
	v_pk_fma_f32 v[24:25], v[12:13], v[68:69], v[24:25] op_sel_hi:[0,1,1]
	s_waitcnt lgkmcnt(0)
	v_pk_fma_f32 v[68:69], v[14:15], v[72:73], v[24:25] op_sel_hi:[0,1,1]
	v_pk_fma_f32 v[24:25], v[4:5], v[30:31], 0 op_sel_hi:[0,1,0]
	v_pk_fma_f32 v[24:25], v[6:7], v[46:47], v[24:25] op_sel_hi:[0,1,1]
	v_pk_fma_f32 v[24:25], v[8:9], v[54:55], v[24:25] op_sel_hi:[0,1,1]
	v_pk_fma_f32 v[24:25], v[10:11], v[66:67], v[24:25] op_sel_hi:[0,1,1]
	v_pk_fma_f32 v[28:29], v[12:13], v[70:71], v[24:25] op_sel_hi:[0,1,1]
	ds_read_b128 v[24:27], v5 offset:3840
	v_pk_fma_f32 v[70:71], v[14:15], v[74:75], v[28:29] op_sel_hi:[0,1,1]
	ds_read_b128 v[28:31], v5 offset:7648
	ds_read_b128 v[32:35], v5 offset:3856
	ds_read_b128 v[40:43], v5 offset:11456
	ds_read_b128 v[44:47], v5 offset:7664
	v_pk_fma_f32 v[36:37], v[4:5], v[36:37], 0 op_sel_hi:[0,1,0]
	s_waitcnt lgkmcnt(4)
	v_pk_fma_f32 v[24:25], v[6:7], v[24:25], v[36:37] op_sel_hi:[0,1,1]
	ds_read_b128 v[48:51], v5 offset:15264
	ds_read_b128 v[52:55], v5 offset:19072
	ds_read_b128 v[56:59], v5 offset:11472
	s_waitcnt lgkmcnt(6)
	v_pk_fma_f32 v[24:25], v[8:9], v[28:29], v[24:25] op_sel_hi:[0,1,1]
	s_waitcnt lgkmcnt(4)
	v_pk_fma_f32 v[24:25], v[10:11], v[40:41], v[24:25] op_sel_hi:[0,1,1]
	s_waitcnt lgkmcnt(2)
	v_pk_fma_f32 v[24:25], v[12:13], v[48:49], v[24:25] op_sel_hi:[0,1,1]
	s_waitcnt lgkmcnt(1)
	v_pk_fma_f32 v[36:37], v[14:15], v[52:53], v[24:25] op_sel_hi:[0,1,1]
	v_pk_fma_f32 v[24:25], v[4:5], v[38:39], 0 op_sel_hi:[0,1,0]
	v_pk_fma_f32 v[24:25], v[6:7], v[26:27], v[24:25] op_sel_hi:[0,1,1]
	v_pk_fma_f32 v[28:29], v[8:9], v[30:31], v[24:25] op_sel_hi:[0,1,1]
	ds_read_b128 v[24:27], v5 offset:22848
	v_pk_fma_f32 v[38:39], v[10:11], v[42:43], v[28:29] op_sel_hi:[0,1,1]
	ds_read_b128 v[28:31], v5 offset:22864
	ds_read_b128 v[60:63], v5 offset:15280
	ds_read_b128 v[64:67], v5 offset:19088
	v_mul_f32_e32 v16, v15, v13
	v_pk_fma_f32 v[0:1], v[4:5], v[0:1], 0 op_sel_hi:[0,1,0]
	s_waitcnt lgkmcnt(3)
	v_pk_fma_f32 v[40:41], v[16:17], v[24:25], v[76:77] op_sel_hi:[0,1,1]
	v_pk_fma_f32 v[78:79], v[16:17], v[26:27], v[78:79] op_sel_hi:[0,1,1]
	s_waitcnt lgkmcnt(2)
	v_pk_fma_f32 v[80:81], v[16:17], v[28:29], v[68:69] op_sel_hi:[0,1,1]
	v_pk_fma_f32 v[82:83], v[16:17], v[30:31], v[70:71] op_sel_hi:[0,1,1]
	v_pk_fma_f32 v[0:1], v[6:7], v[32:33], v[0:1] op_sel_hi:[0,1,1]
	ds_read_b128 v[24:27], v5 offset:22880
	ds_read_b128 v[28:31], v5 offset:22896
	v_pk_fma_f32 v[0:1], v[8:9], v[44:45], v[0:1] op_sel_hi:[0,1,1]
	v_pk_fma_f32 v[0:1], v[10:11], v[56:57], v[0:1] op_sel_hi:[0,1,1]
	s_waitcnt lgkmcnt(3)
	v_pk_fma_f32 v[0:1], v[12:13], v[60:61], v[0:1] op_sel_hi:[0,1,1]
	s_waitcnt lgkmcnt(2)
	v_pk_fma_f32 v[0:1], v[14:15], v[64:65], v[0:1] op_sel_hi:[0,1,1]
	s_waitcnt lgkmcnt(0)
	v_pk_fma_f32 v[88:89], v[16:17], v[28:29], v[0:1] op_sel_hi:[0,1,1]
	v_pk_fma_f32 v[0:1], v[4:5], v[2:3], 0 op_sel_hi:[0,1,0]
	v_pk_fma_f32 v[0:1], v[6:7], v[34:35], v[0:1] op_sel_hi:[0,1,1]
	v_pk_fma_f32 v[0:1], v[8:9], v[46:47], v[0:1] op_sel_hi:[0,1,1]
	v_pk_fma_f32 v[0:1], v[10:11], v[58:59], v[0:1] op_sel_hi:[0,1,1]
	v_pk_fma_f32 v[38:39], v[12:13], v[50:51], v[38:39] op_sel_hi:[0,1,1]
	v_pk_fma_f32 v[84:85], v[16:17], v[24:25], v[36:37] op_sel_hi:[0,1,1]
	v_pk_fma_f32 v[24:25], v[12:13], v[62:63], v[0:1] op_sel_hi:[0,1,1]
	ds_read_b128 v[0:3], v5 offset:64
	v_pk_fma_f32 v[38:39], v[14:15], v[54:55], v[38:39] op_sel_hi:[0,1,1]
	v_pk_fma_f32 v[24:25], v[14:15], v[66:67], v[24:25] op_sel_hi:[0,1,1]
	v_pk_fma_f32 v[86:87], v[16:17], v[26:27], v[38:39] op_sel_hi:[0,1,1]
	v_pk_fma_f32 v[90:91], v[16:17], v[30:31], v[24:25] op_sel_hi:[0,1,1]
	ds_read_b128 v[24:27], v5 offset:3872
	ds_read_b128 v[36:39], v5 offset:80
	ds_read_b128 v[28:31], v5 offset:7680
	ds_read_b128 v[42:45], v5 offset:3888
	ds_read_b128 v[32:35], v5 offset:11488
	ds_read_b128 v[46:49], v5 offset:7696
	s_waitcnt lgkmcnt(6)
	v_pk_fma_f32 v[0:1], v[4:5], v[0:1], 0 op_sel_hi:[0,1,0]
	ds_read_b128 v[50:53], v5 offset:15296
	ds_read_b128 v[54:57], v5 offset:11504
	s_waitcnt lgkmcnt(7)
	v_pk_fma_f32 v[0:1], v[6:7], v[24:25], v[0:1] op_sel_hi:[0,1,1]
	s_waitcnt lgkmcnt(5)
	v_pk_fma_f32 v[0:1], v[8:9], v[28:29], v[0:1] op_sel_hi:[0,1,1]
	ds_read_b128 v[58:61], v5 offset:19104
	ds_read_b128 v[62:65], v5 offset:22912
	ds_read_b128 v[66:69], v5 offset:15312
	s_waitcnt lgkmcnt(6)
	v_pk_fma_f32 v[0:1], v[10:11], v[32:33], v[0:1] op_sel_hi:[0,1,1]
	s_waitcnt lgkmcnt(4)
	v_pk_fma_f32 v[0:1], v[12:13], v[50:51], v[0:1] op_sel_hi:[0,1,1]
	s_waitcnt lgkmcnt(2)
	v_pk_fma_f32 v[0:1], v[14:15], v[58:59], v[0:1] op_sel_hi:[0,1,1]
	s_waitcnt lgkmcnt(1)
	v_pk_fma_f32 v[62:63], v[16:17], v[62:63], v[0:1] op_sel_hi:[0,1,1]
	v_pk_fma_f32 v[0:1], v[4:5], v[2:3], 0 op_sel_hi:[0,1,0]
	v_pk_fma_f32 v[0:1], v[6:7], v[26:27], v[0:1] op_sel_hi:[0,1,1]
	v_pk_fma_f32 v[0:1], v[8:9], v[30:31], v[0:1] op_sel_hi:[0,1,1]
	ds_read_b128 v[74:77], v5 offset:22928
	v_pk_fma_f32 v[24:25], v[10:11], v[34:35], v[0:1] op_sel_hi:[0,1,1]
	ds_read_b128 v[0:3], v5 offset:26656
	ds_read_b128 v[28:31], v5 offset:26672
	ds_read_b128 v[32:35], v5 offset:26688
	v_pk_fma_f32 v[24:25], v[12:13], v[52:53], v[24:25] op_sel_hi:[0,1,1]
	v_mul_f32_e32 v18, v15, v7
	ds_read_b128 v[70:73], v5 offset:19120
	v_pk_fma_f32 v[24:25], v[14:15], v[60:61], v[24:25] op_sel_hi:[0,1,1]
	v_pk_fma_f32 v[36:37], v[4:5], v[36:37], 0 op_sel_hi:[0,1,0]
	v_pk_fma_f32 v[38:39], v[4:5], v[38:39], 0 op_sel_hi:[0,1,0]
	v_pk_fma_f32 v[64:65], v[16:17], v[64:65], v[24:25] op_sel_hi:[0,1,1]
	s_waitcnt lgkmcnt(3)
	v_pk_fma_f32 v[24:25], v[18:19], v[0:1], v[40:41] op_sel_hi:[0,1,1]
	v_pk_fma_f32 v[26:27], v[18:19], v[2:3], v[78:79] op_sel_hi:[0,1,1]
	s_waitcnt lgkmcnt(2)
	v_pk_fma_f32 v[0:1], v[18:19], v[28:29], v[80:81] op_sel_hi:[0,1,1]
	v_pk_fma_f32 v[2:3], v[18:19], v[30:31], v[82:83] op_sel_hi:[0,1,1]
	ds_read_b128 v[28:31], v5 offset:26704
	ds_read_b128 v[50:53], v5 offset:26720
	v_pk_fma_f32 v[36:37], v[6:7], v[42:43], v[36:37] op_sel_hi:[0,1,1]
	v_pk_fma_f32 v[38:39], v[6:7], v[44:45], v[38:39] op_sel_hi:[0,1,1]
	v_pk_fma_f32 v[36:37], v[8:9], v[46:47], v[36:37] op_sel_hi:[0,1,1]
	ds_read_b128 v[58:61], v5 offset:26736
	v_pk_fma_f32 v[38:39], v[8:9], v[48:49], v[38:39] op_sel_hi:[0,1,1]
	v_pk_fma_f32 v[36:37], v[10:11], v[54:55], v[36:37] op_sel_hi:[0,1,1]
	v_pk_fma_f32 v[38:39], v[10:11], v[56:57], v[38:39] op_sel_hi:[0,1,1]
	v_pk_fma_f32 v[36:37], v[12:13], v[66:67], v[36:37] op_sel_hi:[0,1,1]
	v_pk_fma_f32 v[38:39], v[12:13], v[68:69], v[38:39] op_sel_hi:[0,1,1]
	ds_read_b128 v[44:47], v5 offset:96
	s_waitcnt lgkmcnt(4)
	v_pk_fma_f32 v[36:37], v[14:15], v[70:71], v[36:37] op_sel_hi:[0,1,1]
	v_pk_fma_f32 v[38:39], v[14:15], v[72:73], v[38:39] op_sel_hi:[0,1,1]
	v_pk_fma_f32 v[36:37], v[16:17], v[74:75], v[36:37] op_sel_hi:[0,1,1]
	s_waitcnt lgkmcnt(3)
	v_pk_fma_f32 v[40:41], v[18:19], v[28:29], v[88:89] op_sel_hi:[0,1,1]
	v_pk_fma_f32 v[42:43], v[18:19], v[30:31], v[90:91] op_sel_hi:[0,1,1]
	s_waitcnt lgkmcnt(2)
	v_pk_fma_f32 v[30:31], v[18:19], v[50:51], v[62:63] op_sel_hi:[0,1,1]
	v_pk_fma_f32 v[28:29], v[18:19], v[52:53], v[64:65] op_sel_hi:[0,1,1]
	v_pk_fma_f32 v[38:39], v[16:17], v[76:77], v[38:39] op_sel_hi:[0,1,1]
	ds_read_b128 v[48:51], v5 offset:3904
	ds_read_b128 v[52:55], v5 offset:112
	v_pk_fma_f32 v[32:33], v[18:19], v[32:33], v[84:85] op_sel_hi:[0,1,1]
	v_pk_fma_f32 v[34:35], v[18:19], v[34:35], v[86:87] op_sel_hi:[0,1,1]
	s_waitcnt lgkmcnt(3)
	v_pk_fma_f32 v[36:37], v[18:19], v[58:59], v[36:37] op_sel_hi:[0,1,1]
	v_pk_fma_f32 v[38:39], v[18:19], v[60:61], v[38:39] op_sel_hi:[0,1,1]
	ds_read_b128 v[56:59], v5 offset:7712
	ds_read_b128 v[60:63], v5 offset:3920
	ds_read_b128 v[64:67], v5 offset:11520
	ds_read_b128 v[68:71], v5 offset:7728
	ds_read_b128 v[72:75], v5 offset:15328
	ds_read_b128 v[76:79], v5 offset:11536
	ds_read_b128 v[80:83], v5 offset:19136
	ds_read_b128 v[84:87], v5 offset:15344
	ds_read_b128 v[88:91], v5 offset:22944
	ds_read_b128 v[92:95], v5 offset:19152
	ds_read_b128 v[96:99], v5 offset:26752
	ds_read_b128 v[100:103], v5 offset:30464
	ds_read_b128 v[104:107], v5 offset:22960
	s_waitcnt lgkmcnt(14)
	v_pk_fma_f32 v[44:45], v[4:5], v[44:45], 0 op_sel_hi:[0,1,0]
	v_pk_fma_f32 v[44:45], v[6:7], v[48:49], v[44:45] op_sel_hi:[0,1,1]
	ds_read_b128 v[116:119], v5 offset:30496
	s_waitcnt lgkmcnt(13)
	v_pk_fma_f32 v[44:45], v[8:9], v[56:57], v[44:45] op_sel_hi:[0,1,1]
	s_waitcnt lgkmcnt(2)
	v_pk_fma_f32 v[48:49], v[20:21], v[100:101], v[24:25] op_sel_hi:[0,1,1]
	v_pk_fma_f32 v[56:57], v[20:21], v[102:103], v[26:27] op_sel_hi:[0,1,1]
	ds_read_b128 v[24:27], v5 offset:30512
	s_waitcnt lgkmcnt(1)
	v_pk_fma_f32 v[32:33], v[20:21], v[116:117], v[32:33] op_sel_hi:[0,1,1]
	v_pk_fma_f32 v[34:35], v[20:21], v[118:119], v[34:35] op_sel_hi:[0,1,1]
	ds_read_b128 v[108:111], v5 offset:26768
	ds_read_b128 v[112:115], v5 offset:30480
	s_waitcnt lgkmcnt(2)
	v_pk_fma_f32 v[40:41], v[20:21], v[24:25], v[40:41] op_sel_hi:[0,1,1]
	v_cvt_pk_f16_f32 v24, v32, v33
	v_pk_fma_f32 v[32:33], v[4:5], v[46:47], 0 op_sel_hi:[0,1,0]
	v_pk_fma_f32 v[32:33], v[6:7], v[50:51], v[32:33] op_sel_hi:[0,1,1]
	v_pk_fma_f32 v[32:33], v[8:9], v[58:59], v[32:33] op_sel_hi:[0,1,1]
	v_pk_fma_f32 v[32:33], v[10:11], v[66:67], v[32:33] op_sel_hi:[0,1,1]
	v_pk_fma_f32 v[42:43], v[20:21], v[26:27], v[42:43] op_sel_hi:[0,1,1]
	v_cvt_pk_f16_f32 v25, v34, v35
	v_cvt_pk_f16_f32 v26, v40, v41
	v_pk_fma_f32 v[40:41], v[12:13], v[74:75], v[32:33] op_sel_hi:[0,1,1]
	ds_read_b128 v[32:35], v5 offset:30528
	v_pk_fma_f32 v[40:41], v[14:15], v[82:83], v[40:41] op_sel_hi:[0,1,1]
	v_cvt_pk_f16_f32 v27, v42, v43
	v_pk_fma_f32 v[46:47], v[16:17], v[90:91], v[40:41] op_sel_hi:[0,1,1]
	ds_read_b128 v[40:43], v5 offset:30544
	v_pk_fma_f32 v[44:45], v[10:11], v[64:65], v[44:45] op_sel_hi:[0,1,1]
	s_waitcnt lgkmcnt(2)
	v_pk_fma_f32 v[64:65], v[20:21], v[112:113], v[0:1] op_sel_hi:[0,1,1]
	v_cvt_pk_f16_f32 v0, v48, v49
	s_waitcnt lgkmcnt(1)
	v_pk_fma_f32 v[48:49], v[20:21], v[32:33], v[30:31] op_sel_hi:[0,1,1]
	ds_read_b128 v[30:33], v5 offset:30560
	v_pk_fma_f32 v[44:45], v[12:13], v[72:73], v[44:45] op_sel_hi:[0,1,1]
	v_pk_fma_f32 v[44:45], v[14:15], v[80:81], v[44:45] op_sel_hi:[0,1,1]
	v_pk_fma_f32 v[44:45], v[16:17], v[88:89], v[44:45] op_sel_hi:[0,1,1]
	v_pk_fma_f32 v[72:73], v[20:21], v[114:115], v[2:3] op_sel_hi:[0,1,1]
	v_pk_fma_f32 v[44:45], v[18:19], v[96:97], v[44:45] op_sel_hi:[0,1,1]
	v_cvt_pk_f16_f32 v1, v56, v57
	v_cvt_pk_f16_f32 v2, v64, v65
	v_cvt_pk_f16_f32 v3, v72, v73
	v_pk_fma_f32 v[50:51], v[20:21], v[34:35], v[28:29] op_sel_hi:[0,1,1]
	s_waitcnt lgkmcnt(1)
	v_pk_fma_f32 v[40:41], v[20:21], v[40:41], v[36:37] op_sel_hi:[0,1,1]
	v_pk_fma_f32 v[38:39], v[20:21], v[42:43], v[38:39] op_sel_hi:[0,1,1]
	ds_read_b128 v[34:37], v5 offset:30576
	s_waitcnt lgkmcnt(1)
	v_pk_fma_f32 v[42:43], v[20:21], v[30:31], v[44:45] op_sel_hi:[0,1,1]
	v_cvt_pk_f16_f32 v28, v48, v49
	v_cvt_pk_f16_f32 v29, v50, v51
	v_cvt_pk_f16_f32 v30, v40, v41
	v_cvt_pk_f16_f32 v31, v38, v39
	v_pk_fma_f32 v[38:39], v[4:5], v[52:53], 0 op_sel_hi:[0,1,0]
	global_store_dwordx4 v[22:23], v[0:3], off
	global_store_dwordx4 v[22:23], v[24:27], off offset:16
	global_store_dwordx4 v[22:23], v[28:31], off offset:32
	v_pk_fma_f32 v[0:1], v[4:5], v[54:55], 0 op_sel_hi:[0,1,0]
	v_pk_fma_f32 v[38:39], v[6:7], v[60:61], v[38:39] op_sel_hi:[0,1,1]
	v_pk_fma_f32 v[0:1], v[6:7], v[62:63], v[0:1] op_sel_hi:[0,1,1]
	v_pk_fma_f32 v[38:39], v[8:9], v[68:69], v[38:39] op_sel_hi:[0,1,1]
	v_pk_fma_f32 v[0:1], v[8:9], v[70:71], v[0:1] op_sel_hi:[0,1,1]
	v_pk_fma_f32 v[38:39], v[10:11], v[76:77], v[38:39] op_sel_hi:[0,1,1]
	v_pk_fma_f32 v[0:1], v[10:11], v[78:79], v[0:1] op_sel_hi:[0,1,1]
	v_pk_fma_f32 v[38:39], v[12:13], v[84:85], v[38:39] op_sel_hi:[0,1,1]
	v_pk_fma_f32 v[0:1], v[12:13], v[86:87], v[0:1] op_sel_hi:[0,1,1]
	v_pk_fma_f32 v[38:39], v[14:15], v[92:93], v[38:39] op_sel_hi:[0,1,1]
	v_pk_fma_f32 v[0:1], v[14:15], v[94:95], v[0:1] op_sel_hi:[0,1,1]
	v_pk_fma_f32 v[38:39], v[16:17], v[104:105], v[38:39] op_sel_hi:[0,1,1]
	v_pk_fma_f32 v[0:1], v[16:17], v[106:107], v[0:1] op_sel_hi:[0,1,1]
	v_pk_fma_f32 v[46:47], v[18:19], v[98:99], v[46:47] op_sel_hi:[0,1,1]
	v_pk_fma_f32 v[38:39], v[18:19], v[108:109], v[38:39] op_sel_hi:[0,1,1]
	v_pk_fma_f32 v[0:1], v[18:19], v[110:111], v[0:1] op_sel_hi:[0,1,1]
	v_pk_fma_f32 v[44:45], v[20:21], v[32:33], v[46:47] op_sel_hi:[0,1,1]
	s_waitcnt lgkmcnt(0)
	v_pk_fma_f32 v[34:35], v[20:21], v[34:35], v[38:39] op_sel_hi:[0,1,1]
	v_pk_fma_f32 v[0:1], v[20:21], v[36:37], v[0:1] op_sel_hi:[0,1,1]
	v_cvt_pk_f16_f32 v32, v42, v43
	v_cvt_pk_f16_f32 v33, v44, v45
	v_cvt_pk_f16_f32 v34, v34, v35
	v_cvt_pk_f16_f32 v35, v0, v1
	global_store_dwordx4 v[22:23], v[32:35], off offset:48
